# baseline (speedup 1.0000x reference)
.Lgru_loop_b:
.Lgru_loop_b2:
	ds_read_b128 v[190:193], v156 offset:0
	ds_read_b128 v[194:197], v156 offset:1024
	ds_read_b128 v[198:201], v156 offset:2048
	ds_read_b128 v[202:205], v156 offset:3072
	global_load_dwordx4 v[112:115], v[166:167], off offset:-2048
	global_load_dwordx4 v[108:111], v[166:167], off offset:-1024
	global_load_dwordx4 v[104:107], v[166:167], off
	global_load_dwordx4 v[100:103], v[166:167], off offset:1024
	s_waitcnt lgkmcnt(3)
	v_mfma_f32_16x16x32_f16 v[124:127], v[12:15], v[190:193], v[116:119]
	v_mfma_f32_16x16x32_f16 v[128:131], v[28:31], v[190:193], v[120:123]
	v_mfma_f32_16x16x32_f16 v[132:135], v[32:35], v[190:193], v[80:83]
	s_waitcnt lgkmcnt(2)
	v_mfma_f32_16x16x32_f16 v[124:127], v[16:19], v[194:197], v[124:127]
	v_mfma_f32_16x16x32_f16 v[128:131], v[48:51], v[194:197], v[128:131]
	v_mfma_f32_16x16x32_f16 v[132:135], v[36:39], v[194:197], v[132:135]
	s_waitcnt lgkmcnt(1)
	v_mfma_f32_16x16x32_f16 v[124:127], v[20:23], v[198:201], v[124:127]
	v_mfma_f32_16x16x32_f16 v[128:131], v[52:55], v[198:201], v[128:131]
	v_mfma_f32_16x16x32_f16 v[132:135], v[40:43], v[198:201], v[132:135]
	s_waitcnt lgkmcnt(0)
	v_mfma_f32_16x16x32_f16 v[124:127], v[24:27], v[202:205], v[124:127]
	v_mfma_f32_16x16x32_f16 v[128:131], v[56:59], v[202:205], v[128:131]
	v_mfma_f32_16x16x32_f16 v[132:135], v[44:47], v[202:205], v[132:135]
	v_exp_f32_e32 v228, v144
	v_exp_f32_e32 v229, v145
	v_exp_f32_e32 v230, v146
	v_exp_f32_e32 v231, v147
	v_exp_f32_e32 v232, v148
	v_exp_f32_e32 v233, v149
	v_exp_f32_e32 v234, v150
	v_exp_f32_e32 v235, v151
	v_add_f32_e32 v228, 1.0, v228
	v_add_f32_e32 v229, 1.0, v229
	v_add_f32_e32 v230, 1.0, v230
	v_add_f32_e32 v231, 1.0, v231
	v_add_f32_e32 v232, 1.0, v232
	v_add_f32_e32 v233, 1.0, v233
	v_add_f32_e32 v234, 1.0, v234
	v_add_f32_e32 v235, 1.0, v235
	v_rcp_f32_e32 v228, v228
	v_rcp_f32_e32 v229, v229
	v_rcp_f32_e32 v230, v230
	v_rcp_f32_e32 v231, v231
	v_fma_f32 v236, v228, v152, v182
	v_fma_f32 v237, v229, v153, v183
	v_fma_f32 v238, v230, v154, v184
	v_fma_f32 v239, v231, v155, v185
	v_mad_u32_u24 v227, v177, s17, v226
	ds_read_b128 v[222:225], v227 offset:24848
	ds_read_b128 v[186:189], v227 offset:24864
	ds_read_b128 v[182:185], v227 offset:24880
	ds_read_u16 v177, v176 offset:4162
	v_exp_f32_e32 v236, v236
	v_exp_f32_e32 v237, v237
	v_exp_f32_e32 v238, v238
	v_exp_f32_e32 v239, v239
	v_rcp_f32_e32 v232, v232
	v_rcp_f32_e32 v233, v233
	v_rcp_f32_e32 v234, v234
	v_rcp_f32_e32 v235, v235
	v_add_f32_e32 v236, 1.0, v236
	v_add_f32_e32 v237, 1.0, v237
	v_add_f32_e32 v238, 1.0, v238
	v_add_f32_e32 v239, 1.0, v239
	v_rcp_f32_e32 v236, v236
	v_rcp_f32_e32 v237, v237
	v_rcp_f32_e32 v238, v238
	v_rcp_f32_e32 v239, v239
	v_pk_fma_f32 v[236:237], v[236:237], -2.0, 1.0 op_sel_hi:[1,0,0]
	v_pk_fma_f32 v[238:239], v[238:239], -2.0, 1.0 op_sel_hi:[1,0,0]
	v_pk_add_f32 v[240:241], v[168:169], v[236:237] neg_lo:[0,1] neg_hi:[0,1]
	v_pk_add_f32 v[242:243], v[170:171], v[238:239] neg_lo:[0,1] neg_hi:[0,1]
	v_pk_fma_f32 v[168:169], v[232:233], v[240:241], v[236:237]
	v_pk_fma_f32 v[170:171], v[234:235], v[242:243], v[238:239]
	v_cvt_pk_f16_f32 v244, v168, v169
	v_cvt_pk_f16_f32 v245, v170, v171
	ds_write_b64 v163, v[244:245] offset:4096
	s_waitcnt vmcnt(4)
	v_mfma_f32_16x16x32_f16 v[96:99], v[72:75], v[190:193], v[96:99]
	v_mfma_f32_16x16x32_f16 v[96:99], v[8:11], v[194:197], v[96:99]
	v_mfma_f32_16x16x32_f16 v[96:99], v[4:7], v[198:201], v[96:99]
	v_mfma_f32_16x16x32_f16 v[96:99], v[0:3], v[202:205], v[96:99]
	s_waitcnt lgkmcnt(0)
	s_barrier
	s_nop 0
	ds_read_b128 v[206:209], v156 offset:4096
	ds_read_b128 v[210:213], v156 offset:5120
	ds_read_b128 v[214:217], v156 offset:6144
	ds_read_b128 v[218:221], v156 offset:7168
	s_waitcnt lgkmcnt(3)
	v_mfma_f32_16x16x32_f16 v[144:147], v[12:15], v[206:209], v[222:225]
	v_mfma_f32_16x16x32_f16 v[148:151], v[28:31], v[206:209], v[186:189]
	v_mfma_f32_16x16x32_f16 v[152:155], v[32:35], v[206:209], v[80:83]
	s_waitcnt lgkmcnt(2)
	v_mfma_f32_16x16x32_f16 v[144:147], v[16:19], v[210:213], v[144:147]
	v_mfma_f32_16x16x32_f16 v[148:151], v[48:51], v[210:213], v[148:151]
	v_mfma_f32_16x16x32_f16 v[152:155], v[36:39], v[210:213], v[152:155]
	s_waitcnt lgkmcnt(1)
	v_mfma_f32_16x16x32_f16 v[144:147], v[20:23], v[214:217], v[144:147]
	v_mfma_f32_16x16x32_f16 v[148:151], v[52:55], v[214:217], v[148:151]
	v_mfma_f32_16x16x32_f16 v[152:155], v[40:43], v[214:217], v[152:155]
	s_waitcnt lgkmcnt(0)
	v_mfma_f32_16x16x32_f16 v[144:147], v[24:27], v[218:221], v[144:147]
	v_mfma_f32_16x16x32_f16 v[148:151], v[56:59], v[218:221], v[148:151]
	v_mfma_f32_16x16x32_f16 v[152:155], v[44:47], v[218:221], v[152:155]
	v_exp_f32_e32 v228, v124
	v_exp_f32_e32 v229, v125
	v_exp_f32_e32 v230, v126
	v_exp_f32_e32 v231, v127
	v_exp_f32_e32 v232, v128
	v_exp_f32_e32 v233, v129
	v_exp_f32_e32 v234, v130
	v_exp_f32_e32 v235, v131
	v_add_f32_e32 v228, 1.0, v228
	v_add_f32_e32 v229, 1.0, v229
	v_add_f32_e32 v230, 1.0, v230
	v_add_f32_e32 v231, 1.0, v231
	v_add_f32_e32 v232, 1.0, v232
	v_add_f32_e32 v233, 1.0, v233
	v_add_f32_e32 v234, 1.0, v234
	v_add_f32_e32 v235, 1.0, v235
	v_rcp_f32_e32 v228, v228
	v_rcp_f32_e32 v229, v229
	v_rcp_f32_e32 v230, v230
	v_rcp_f32_e32 v231, v231
	v_fma_f32 v236, v228, v132, v138
	v_fma_f32 v237, v229, v133, v139
	v_fma_f32 v238, v230, v134, v140
	v_fma_f32 v239, v231, v135, v141
	v_mad_u32_u24 v227, v178, s17, v226
	ds_read_b128 v[116:119], v227 offset:24848
	ds_read_b128 v[120:123], v227 offset:24864
	ds_read_b128 v[138:141], v227 offset:24880
	ds_read_u16 v178, v176 offset:4
	v_exp_f32_e32 v236, v236
	v_exp_f32_e32 v237, v237
	v_exp_f32_e32 v238, v238
	v_exp_f32_e32 v239, v239
	v_rcp_f32_e32 v232, v232
	v_rcp_f32_e32 v233, v233
	v_rcp_f32_e32 v234, v234
	v_rcp_f32_e32 v235, v235
	v_add_f32_e32 v236, 1.0, v236
	v_add_f32_e32 v237, 1.0, v237
	v_add_f32_e32 v238, 1.0, v238
	v_add_f32_e32 v239, 1.0, v239
	v_rcp_f32_e32 v236, v236
	v_rcp_f32_e32 v237, v237
	v_rcp_f32_e32 v238, v238
	v_rcp_f32_e32 v239, v239
	v_pk_fma_f32 v[236:237], v[236:237], -2.0, 1.0 op_sel_hi:[1,0,0]
	v_pk_fma_f32 v[238:239], v[238:239], -2.0, 1.0 op_sel_hi:[1,0,0]
	v_pk_add_f32 v[240:241], v[172:173], v[236:237] neg_lo:[0,1] neg_hi:[0,1]
	v_pk_add_f32 v[242:243], v[174:175], v[238:239] neg_lo:[0,1] neg_hi:[0,1]
	v_pk_fma_f32 v[172:173], v[232:233], v[240:241], v[236:237]
	v_pk_fma_f32 v[174:175], v[234:235], v[242:243], v[238:239]
	v_cvt_pk_f16_f32 v244, v172, v173
	v_cvt_pk_f16_f32 v245, v174, v175
	ds_write_b64 v163, v[244:245]
	s_waitcnt vmcnt(4)
	v_mfma_f32_16x16x32_f16 v[92:95], v[72:75], v[206:209], v[92:95]
	v_mfma_f32_16x16x32_f16 v[92:95], v[8:11], v[210:213], v[92:95]
	v_mfma_f32_16x16x32_f16 v[92:95], v[4:7], v[214:217], v[92:95]
	v_mfma_f32_16x16x32_f16 v[92:95], v[0:3], v[218:221], v[92:95]
	s_waitcnt lgkmcnt(0)
	s_barrier
	s_nop 0
	ds_read_b128 v[190:193], v156 offset:0
	ds_read_b128 v[194:197], v156 offset:1024
	ds_read_b128 v[198:201], v156 offset:2048
	ds_read_b128 v[202:205], v156 offset:3072
	s_ashr_i32 s9, s8, 31
	s_lshl_b64 s[12:13], s[8:9], 15
	v_lshl_add_u64 v[246:247], v[158:159], 0, s[12:13]
	global_load_dwordx4 v[72:75], v[246:247], off
	global_load_dwordx4 v[8:11], v[246:247], off offset:1024
	global_load_dwordx4 v[4:7], v[246:247], off offset:2048
	global_load_dwordx4 v[0:3], v[246:247], off offset:3072
	s_waitcnt lgkmcnt(3)
	v_mfma_f32_16x16x32_f16 v[124:127], v[12:15], v[190:193], v[116:119]
	v_mfma_f32_16x16x32_f16 v[128:131], v[28:31], v[190:193], v[120:123]
	v_mfma_f32_16x16x32_f16 v[132:135], v[32:35], v[190:193], v[80:83]
	s_waitcnt lgkmcnt(2)
	v_mfma_f32_16x16x32_f16 v[124:127], v[16:19], v[194:197], v[124:127]
	v_mfma_f32_16x16x32_f16 v[128:131], v[48:51], v[194:197], v[128:131]
	v_mfma_f32_16x16x32_f16 v[132:135], v[36:39], v[194:197], v[132:135]
	s_waitcnt lgkmcnt(1)
	v_mfma_f32_16x16x32_f16 v[124:127], v[20:23], v[198:201], v[124:127]
	v_mfma_f32_16x16x32_f16 v[128:131], v[52:55], v[198:201], v[128:131]
	v_mfma_f32_16x16x32_f16 v[132:135], v[40:43], v[198:201], v[132:135]
	s_waitcnt lgkmcnt(0)
	v_mfma_f32_16x16x32_f16 v[124:127], v[24:27], v[202:205], v[124:127]
	v_mfma_f32_16x16x32_f16 v[128:131], v[56:59], v[202:205], v[128:131]
	v_mfma_f32_16x16x32_f16 v[132:135], v[44:47], v[202:205], v[132:135]
	v_exp_f32_e32 v228, v144
	v_exp_f32_e32 v229, v145
	v_exp_f32_e32 v230, v146
	v_exp_f32_e32 v231, v147
	v_exp_f32_e32 v232, v148
	v_exp_f32_e32 v233, v149
	v_exp_f32_e32 v234, v150
	v_exp_f32_e32 v235, v151
	v_add_f32_e32 v228, 1.0, v228
	v_add_f32_e32 v229, 1.0, v229
	v_add_f32_e32 v230, 1.0, v230
	v_add_f32_e32 v231, 1.0, v231
	v_add_f32_e32 v232, 1.0, v232
	v_add_f32_e32 v233, 1.0, v233
	v_add_f32_e32 v234, 1.0, v234
	v_add_f32_e32 v235, 1.0, v235
	v_rcp_f32_e32 v228, v228
	v_rcp_f32_e32 v229, v229
	v_rcp_f32_e32 v230, v230
	v_rcp_f32_e32 v231, v231
	v_fma_f32 v236, v228, v152, v182
	v_fma_f32 v237, v229, v153, v183
	v_fma_f32 v238, v230, v154, v184
	v_fma_f32 v239, v231, v155, v185
	v_mad_u32_u24 v227, v177, s17, v226
	ds_read_b128 v[222:225], v227 offset:24848
	ds_read_b128 v[186:189], v227 offset:24864
	ds_read_b128 v[182:185], v227 offset:24880
	ds_read_u16 v177, v176 offset:4164
	v_exp_f32_e32 v236, v236
	v_exp_f32_e32 v237, v237
	v_exp_f32_e32 v238, v238
	v_exp_f32_e32 v239, v239
	v_rcp_f32_e32 v232, v232
	v_rcp_f32_e32 v233, v233
	v_rcp_f32_e32 v234, v234
	v_rcp_f32_e32 v235, v235
	v_add_f32_e32 v236, 1.0, v236
	v_add_f32_e32 v237, 1.0, v237
	v_add_f32_e32 v238, 1.0, v238
	v_add_f32_e32 v239, 1.0, v239
	v_rcp_f32_e32 v236, v236
	v_rcp_f32_e32 v237, v237
	v_rcp_f32_e32 v238, v238
	v_rcp_f32_e32 v239, v239
	v_pk_fma_f32 v[236:237], v[236:237], -2.0, 1.0 op_sel_hi:[1,0,0]
	v_pk_fma_f32 v[238:239], v[238:239], -2.0, 1.0 op_sel_hi:[1,0,0]
	v_pk_add_f32 v[240:241], v[168:169], v[236:237] neg_lo:[0,1] neg_hi:[0,1]
	v_pk_add_f32 v[242:243], v[170:171], v[238:239] neg_lo:[0,1] neg_hi:[0,1]
	v_pk_fma_f32 v[168:169], v[232:233], v[240:241], v[236:237]
	v_pk_fma_f32 v[170:171], v[234:235], v[242:243], v[238:239]
	v_cvt_pk_f16_f32 v244, v168, v169
	v_cvt_pk_f16_f32 v245, v170, v171
	ds_write_b64 v163, v[244:245] offset:4096
	s_waitcnt vmcnt(4)
	v_mfma_f32_16x16x32_f16 v[96:99], v[112:115], v[190:193], v[96:99]
	v_mfma_f32_16x16x32_f16 v[96:99], v[108:111], v[194:197], v[96:99]
	v_mfma_f32_16x16x32_f16 v[96:99], v[104:107], v[198:201], v[96:99]
	v_mfma_f32_16x16x32_f16 v[96:99], v[100:103], v[202:205], v[96:99]
	s_waitcnt lgkmcnt(0)
	s_barrier
	s_nop 0
	ds_read_b128 v[206:209], v156 offset:4096
	ds_read_b128 v[210:213], v156 offset:5120
	ds_read_b128 v[214:217], v156 offset:6144
	ds_read_b128 v[218:221], v156 offset:7168
	s_waitcnt lgkmcnt(3)
	v_mfma_f32_16x16x32_f16 v[144:147], v[12:15], v[206:209], v[222:225]
	v_mfma_f32_16x16x32_f16 v[148:151], v[28:31], v[206:209], v[186:189]
	v_mfma_f32_16x16x32_f16 v[152:155], v[32:35], v[206:209], v[80:83]
	s_waitcnt lgkmcnt(2)
	v_mfma_f32_16x16x32_f16 v[144:147], v[16:19], v[210:213], v[144:147]
	v_mfma_f32_16x16x32_f16 v[148:151], v[48:51], v[210:213], v[148:151]
	v_mfma_f32_16x16x32_f16 v[152:155], v[36:39], v[210:213], v[152:155]
	s_waitcnt lgkmcnt(1)
	v_mfma_f32_16x16x32_f16 v[144:147], v[20:23], v[214:217], v[144:147]
	v_mfma_f32_16x16x32_f16 v[148:151], v[52:55], v[214:217], v[148:151]
	v_mfma_f32_16x16x32_f16 v[152:155], v[40:43], v[214:217], v[152:155]
	s_waitcnt lgkmcnt(0)
	v_mfma_f32_16x16x32_f16 v[144:147], v[24:27], v[218:221], v[144:147]
	v_mfma_f32_16x16x32_f16 v[148:151], v[56:59], v[218:221], v[148:151]
	v_mfma_f32_16x16x32_f16 v[152:155], v[44:47], v[218:221], v[152:155]
	v_exp_f32_e32 v228, v124
	v_exp_f32_e32 v229, v125
	v_exp_f32_e32 v230, v126
	v_exp_f32_e32 v231, v127
	v_exp_f32_e32 v232, v128
	v_exp_f32_e32 v233, v129
	v_exp_f32_e32 v234, v130
	v_exp_f32_e32 v235, v131
	v_add_f32_e32 v228, 1.0, v228
	v_add_f32_e32 v229, 1.0, v229
	v_add_f32_e32 v230, 1.0, v230
	v_add_f32_e32 v231, 1.0, v231
	v_add_f32_e32 v232, 1.0, v232
	v_add_f32_e32 v233, 1.0, v233
	v_add_f32_e32 v234, 1.0, v234
	v_add_f32_e32 v235, 1.0, v235
	v_rcp_f32_e32 v228, v228
	v_rcp_f32_e32 v229, v229
	v_rcp_f32_e32 v230, v230
	v_rcp_f32_e32 v231, v231
	v_fma_f32 v236, v228, v132, v138
	v_fma_f32 v237, v229, v133, v139
	v_fma_f32 v238, v230, v134, v140
	v_fma_f32 v239, v231, v135, v141
	v_mad_u32_u24 v227, v178, s17, v226
	ds_read_b128 v[116:119], v227 offset:24848
	ds_read_b128 v[120:123], v227 offset:24864
	ds_read_b128 v[138:141], v227 offset:24880
	ds_read_u16 v178, v176 offset:6
	v_exp_f32_e32 v236, v236
	v_exp_f32_e32 v237, v237
	v_exp_f32_e32 v238, v238
	v_exp_f32_e32 v239, v239
	v_rcp_f32_e32 v232, v232
	v_rcp_f32_e32 v233, v233
	v_rcp_f32_e32 v234, v234
	v_rcp_f32_e32 v235, v235
	v_add_f32_e32 v236, 1.0, v236
	v_add_f32_e32 v237, 1.0, v237
	v_add_f32_e32 v238, 1.0, v238
	v_add_f32_e32 v239, 1.0, v239
	v_rcp_f32_e32 v236, v236
	v_rcp_f32_e32 v237, v237
	v_rcp_f32_e32 v238, v238
	v_rcp_f32_e32 v239, v239
	v_pk_fma_f32 v[236:237], v[236:237], -2.0, 1.0 op_sel_hi:[1,0,0]
	v_pk_fma_f32 v[238:239], v[238:239], -2.0, 1.0 op_sel_hi:[1,0,0]
	v_pk_add_f32 v[240:241], v[172:173], v[236:237] neg_lo:[0,1] neg_hi:[0,1]
	v_pk_add_f32 v[242:243], v[174:175], v[238:239] neg_lo:[0,1] neg_hi:[0,1]
	v_pk_fma_f32 v[172:173], v[232:233], v[240:241], v[236:237]
	v_pk_fma_f32 v[174:175], v[234:235], v[242:243], v[238:239]
	v_cvt_pk_f16_f32 v244, v172, v173
	v_cvt_pk_f16_f32 v245, v174, v175
	ds_write_b64 v163, v[244:245]
	s_waitcnt vmcnt(4)
	v_mfma_f32_16x16x32_f16 v[92:95], v[112:115], v[206:209], v[92:95]
	v_mfma_f32_16x16x32_f16 v[92:95], v[108:111], v[210:213], v[92:95]
	v_mfma_f32_16x16x32_f16 v[92:95], v[104:107], v[214:217], v[92:95]
	v_mfma_f32_16x16x32_f16 v[92:95], v[100:103], v[218:221], v[92:95]
	s_add_i32 s5, s5, 2
	s_add_i32 s8, s8, s4
	v_add_u32_e32 v176, 4, v176
	v_lshl_add_u64 v[166:167], v[166:167], 0, s[6:7]
	s_cmpk_gt_u32 s5, 0x7d
	s_waitcnt lgkmcnt(0)
	s_barrier
	s_cbranch_scc0 .Lgru_loop_b2
	s_waitcnt vmcnt(0)
	s_branch .Lgru_tail2
